# batched the global loads of six LDS table-copy loops (router weights, DFT tables, twiddles, rope tables, LN gain/bias); attention loop trims
# speedup vs baseline: 1.0088x; 1.0088x over previous
.LBB0_266:
	v_ashrrev_i32_e32 v5, 4, v4
	v_lshl_or_b32 v6, v5, 11, v1
	v_ashrrev_i32_e32 v7, 31, v6
	v_lshl_add_u64 v[8:9], v[6:7], 2, s[14:15]
	global_load_dword v10, v[8:9], off
	v_add_u32_e32 v6, 0x20000, v6
	v_ashrrev_i32_e32 v7, 31, v6
	v_lshl_add_u64 v[8:9], v[6:7], 2, s[14:15]
	global_load_dword v11, v[8:9], off
	v_lshl_or_b32 v6, v5, 5, v1
	v_ashrrev_i32_e32 v7, 31, v6
	v_lshl_add_u64 v[8:9], v[6:7], 2, s[14:15]
	global_load_dword v12, v[8:9], off offset:64
	v_add_u32_e32 v6, 0x20010, v6
	v_ashrrev_i32_e32 v7, 31, v6
	v_lshl_add_u64 v[8:9], v[6:7], 2, s[14:15]
	global_load_dword v13, v[8:9], off
	v_add_u32_e32 v5, 32, v5
	v_lshl_or_b32 v6, v5, 11, v1
	v_ashrrev_i32_e32 v7, 31, v6
	v_lshl_add_u64 v[8:9], v[6:7], 2, s[14:15]
	global_load_dword v14, v[8:9], off
	v_add_u32_e32 v6, 0x20000, v6
	v_ashrrev_i32_e32 v7, 31, v6
	v_lshl_add_u64 v[8:9], v[6:7], 2, s[14:15]
	global_load_dword v15, v[8:9], off
	v_lshl_or_b32 v6, v5, 5, v1
	v_ashrrev_i32_e32 v7, 31, v6
	v_lshl_add_u64 v[8:9], v[6:7], 2, s[14:15]
	global_load_dword v16, v[8:9], off offset:64
	v_add_u32_e32 v6, 0x20010, v6
	v_ashrrev_i32_e32 v7, 31, v6
	v_lshl_add_u64 v[8:9], v[6:7], 2, s[14:15]
	global_load_dword v17, v[8:9], off
	s_waitcnt vmcnt(6)
	ds_write2st64_b32 v2, v10, v11 offset1:16
	s_waitcnt vmcnt(4)
	ds_write2st64_b32 v2, v12, v13 offset0:32 offset1:48
	v_add_u32_e32 v2, 0x800, v2
	s_waitcnt vmcnt(2)
	ds_write2st64_b32 v2, v14, v15 offset1:16
	s_waitcnt vmcnt(0)
	ds_write2st64_b32 v2, v16, v17 offset0:32 offset1:48

.LBB0_293:
	global_load_dwordx4 v[8:11], v[4:5], off
	v_lshl_add_u64 v[4:5], v[4:5], 0, s[94:95]
	global_load_dwordx4 v[12:15], v[4:5], off
	v_lshl_add_u64 v[4:5], v[4:5], 0, s[94:95]
	global_load_dwordx4 v[16:19], v[4:5], off
	v_lshl_add_u64 v[4:5], v[4:5], 0, s[94:95]
	v_cmp_gt_i32_e32 vcc, 0xc0, v230
	s_and_saveexec_b64 s[12:13], vcc
	global_load_dwordx4 v[20:23], v[4:5], off
	s_mov_b64 exec, s[12:13]
	s_waitcnt vmcnt(3)
	ds_write_b128 v6, v[8:11]
	s_waitcnt vmcnt(2)
	ds_write_b128 v6, v[12:15] offset:8192
	s_waitcnt vmcnt(1)
	ds_write_b128 v6, v[16:19] offset:16384
	s_and_saveexec_b64 s[12:13], vcc
	s_waitcnt vmcnt(0)
	ds_write_b128 v6, v[20:23] offset:24576
	s_mov_b64 exec, s[12:13]

.LBB0_296:
	global_load_dwordx4 v[8:11], v[4:5], off
	v_lshl_add_u64 v[4:5], v[4:5], 0, s[94:95]
	global_load_dwordx4 v[12:15], v[4:5], off
	v_lshl_add_u64 v[4:5], v[4:5], 0, s[94:95]
	global_load_dwordx4 v[16:19], v[4:5], off
	v_lshl_add_u64 v[4:5], v[4:5], 0, s[94:95]
	global_load_dwordx4 v[20:23], v[4:5], off
	s_waitcnt vmcnt(3)
	ds_write_b128 v2, v[8:11]
	s_waitcnt vmcnt(2)
	ds_write_b128 v2, v[12:15] offset:8192
	s_waitcnt vmcnt(1)
	ds_write_b128 v2, v[16:19] offset:16384
	s_waitcnt vmcnt(0)
	ds_write_b128 v2, v[20:23] offset:24576

.LBB0_437:
	global_load_dwordx4 v[6:9], v[4:5], off
	v_lshl_add_u64 v[4:5], v[4:5], 0, s[94:95]
	global_load_dwordx4 v[10:13], v[4:5], off
	v_lshl_add_u64 v[4:5], v[4:5], 0, s[94:95]
	global_load_dwordx4 v[14:17], v[4:5], off
	v_lshl_add_u64 v[4:5], v[4:5], 0, s[94:95]
	v_cmp_gt_i32_e32 vcc, 0xc0, v20
	s_and_saveexec_b64 s[10:11], vcc
	global_load_dwordx4 v[24:27], v[4:5], off
	s_mov_b64 exec, s[10:11]
	s_waitcnt vmcnt(3)
	ds_write_b128 v2, v[6:9]
	s_waitcnt vmcnt(2)
	ds_write_b128 v2, v[10:13] offset:8192
	s_waitcnt vmcnt(1)
	ds_write_b128 v2, v[14:17] offset:16384
	s_and_saveexec_b64 s[10:11], vcc
	s_waitcnt vmcnt(0)
	ds_write_b128 v2, v[24:27] offset:24576
	s_mov_b64 exec, s[10:11]

.LBB0_722:
	v_lshrrev_b32_e32 v10, 7, v2
	v_and_b32_e32 v11, 0xfffff80, v2
	v_xor_b32_e32 v12, v10, v1
	v_or_b32_e32 v13, 4, v10
	v_xor_b32_e32 v13, v13, v1
	v_lshlrev_b32_e32 v11, 4, v11
	v_lshl_add_u32 v12, v12, 4, v11
	v_lshl_add_u32 v13, v13, 4, v11
	v_add_u32_e32 v14, 0x10000, v12
	v_add_u32_e32 v15, 0x10000, v13
	global_load_dwordx4 v[16:19], v[4:5], off
	v_lshl_add_u64 v[4:5], v[4:5], 0, s[94:95]
	global_load_dwordx4 v[20:23], v[4:5], off
	v_lshl_add_u64 v[4:5], v[4:5], 0, s[94:95]
	global_load_dwordx4 v[24:27], v[4:5], off
	v_lshl_add_u64 v[4:5], v[4:5], 0, s[94:95]
	global_load_dwordx4 v[28:31], v[4:5], off
	v_lshl_add_u64 v[4:5], v[4:5], 0, s[94:95]
	global_load_dwordx4 v[32:35], v[4:5], off
	v_lshl_add_u64 v[4:5], v[4:5], 0, s[94:95]
	global_load_dwordx4 v[36:39], v[4:5], off
	v_lshl_add_u64 v[4:5], v[4:5], 0, s[94:95]
	global_load_dwordx4 v[40:43], v[4:5], off
	v_lshl_add_u64 v[4:5], v[4:5], 0, s[94:95]
	global_load_dwordx4 v[44:47], v[4:5], off
	v_lshl_add_u64 v[4:5], v[4:5], 0, s[94:95]
	global_load_dwordx4 v[48:51], v[4:5], off
	v_lshl_add_u64 v[4:5], v[4:5], 0, s[94:95]
	global_load_dwordx4 v[52:55], v[4:5], off
	v_lshl_add_u64 v[4:5], v[4:5], 0, s[94:95]
	global_load_dwordx4 v[56:59], v[4:5], off
	v_lshl_add_u64 v[4:5], v[4:5], 0, s[94:95]
	global_load_dwordx4 v[60:63], v[4:5], off
	v_lshl_add_u64 v[4:5], v[4:5], 0, s[94:95]
	global_load_dwordx4 v[64:67], v[4:5], off
	v_lshl_add_u64 v[4:5], v[4:5], 0, s[94:95]
	global_load_dwordx4 v[68:71], v[4:5], off
	v_lshl_add_u64 v[4:5], v[4:5], 0, s[94:95]
	global_load_dwordx4 v[72:75], v[4:5], off
	v_lshl_add_u64 v[4:5], v[4:5], 0, s[94:95]
	global_load_dwordx4 v[76:79], v[4:5], off
	s_waitcnt vmcnt(15)
	ds_write_b128 v12, v[16:19]
	s_waitcnt vmcnt(14)
	ds_write_b128 v13, v[20:23] offset:8192
	s_waitcnt vmcnt(13)
	ds_write_b128 v12, v[24:27] offset:16384
	s_waitcnt vmcnt(12)
	ds_write_b128 v13, v[28:31] offset:24576
	s_waitcnt vmcnt(11)
	ds_write_b128 v12, v[32:35] offset:32768
	s_waitcnt vmcnt(10)
	ds_write_b128 v13, v[36:39] offset:40960
	s_waitcnt vmcnt(9)
	ds_write_b128 v12, v[40:43] offset:49152
	s_waitcnt vmcnt(8)
	ds_write_b128 v13, v[44:47] offset:57344
	s_waitcnt vmcnt(7)
	ds_write_b128 v14, v[48:51]
	s_waitcnt vmcnt(6)
	ds_write_b128 v15, v[52:55] offset:8192
	s_waitcnt vmcnt(5)
	ds_write_b128 v14, v[56:59] offset:16384
	s_waitcnt vmcnt(4)
	ds_write_b128 v15, v[60:63] offset:24576
	s_waitcnt vmcnt(3)
	ds_write_b128 v14, v[64:67] offset:32768
	s_waitcnt vmcnt(2)
	ds_write_b128 v15, v[68:71] offset:40960
	s_waitcnt vmcnt(1)
	ds_write_b128 v14, v[72:75] offset:49152
	s_waitcnt vmcnt(0)
	ds_write_b128 v15, v[76:79] offset:57344

.LBB0_737:
	global_load_dword v8, v[4:5], off
	global_load_dword v10, v[6:7], off
	v_lshl_add_u64 v[4:5], v[4:5], 0, s[68:69]
	v_lshl_add_u64 v[6:7], v[6:7], 0, s[68:69]
	global_load_dword v11, v[4:5], off
	global_load_dword v12, v[6:7], off
	v_add_u32_e32 v9, 0xfffff000, v2
	s_waitcnt vmcnt(3)
	ds_write_b32 v9, v8
	s_waitcnt vmcnt(2)
	ds_write_b32 v2, v10
	s_waitcnt vmcnt(1)
	ds_write_b32 v9, v11 offset:2048
	s_waitcnt vmcnt(0)
	ds_write_b32 v2, v12 offset:2048
